# MoE gate/up tile prologue: the redundant third workgroup barrier before the first DMA group removed
# baseline (speedup 1.0000x reference)
;     template <class T> __device__ __forceinline__ T* w(size_t off) const { return (T*)(p->ws + off); }
;     ...
;     unsigned ao[4];
; #pragma unroll
;     for (int i = 0; i < 4; ++i) ao[i] = arow((tid >> 3) + 32 * i) + (tid & 7) * 8;
;     const int bk = tid >> 4, bnc = tid & 15;
;     constexpr int NRB = B_F32 ? 8 : 4;
;     u32x4 ra0[4], ra1[4]; u32x4 rb0[NRB], rb1[NRB];
;     auto gloadA = [&](int kt, u32x4 (&ra)[4]) __attribute__((always_inline)) {
; #pragma unroll
;         for (int i = 0; i < 4; ++i) ra[i] = *(const u32x4*)(Abase + (ao[i] + kt * 64));
; __device__ __forceinline__ void ph_moe1_mfma(const Ctx& c, int layer, int tile, const int* sm, unsigned char* lds) {
;     const int st = tile >> 3, nt = tile & 7;
;     const int s0 = st * 128;
;     if (s0 >= sm[32]) return;
;     unsigned* flag = c.w<unsigned>(WS_CTL) + CW_MOEF + (layer * 512 + st) * 16;
;     const int e = slot_expert(sm, s0), base = s0 - sm[e], ce = sm[33 + e];
;     if (base >= ce) { if (c.tid == 0) (void)__hip_atomic_fetch_add(flag, 1u, __ATOMIC_RELAXED, __HIP_MEMORY_SCOPE_AGENT); return; }
;     const bf16* HA = c.w<bf16>(WS_HA); const int* LI = c.w<int>(WS_LIST) + (size_t)e * NT;
;     f32x4 acc[4][4];
;     gemm_tile<false>(c.tid, lds, HA, [&](int r) __attribute__((always_inline)) { const int tok = LI[(base + r < ce) ? (base + r) : base]; return (unsigned)(tok * D); }, c.w<bf16>(WS_BGU) + (size_t)e * D * 1024, (unsigned)(nt * 128 + (c.tid & 15) * 8), 1024, true, D, acc);
.LBB0_162:
	s_and_b32 s7, s58, 7
	s_and_b32 s6, s59, 7
	s_lshl_b32 s15, s7, 7
	v_ashrrev_i32_e32 v4, 3, v118
	s_add_u32 s28, s42, 0x45c6000
	v_add_u32_e32 v4, v2, v4
	s_addc_u32 s29, s43, 0
	s_mul_i32 s7, s18, 0x11000
	v_cmp_lt_i32_e32 vcc, v4, v5
	v_add_u32_e32 v8, 32, v4
	s_add_u32 s7, s42, s7
	v_cndmask_b32_e32 v6, v2, v4, vcc
	v_cmp_lt_i32_e32 vcc, v8, v5
	v_add_u32_e32 v10, 64, v4
	s_addc_u32 s19, s43, 0
	v_cndmask_b32_e32 v8, v2, v8, vcc
	v_cmp_lt_i32_e32 vcc, v10, v5
	v_add_u32_e32 v4, 0x60, v4
	s_add_u32 s44, s7, 0x1012c000
	v_cndmask_b32_e32 v10, v2, v10, vcc
	v_cmp_lt_i32_e32 vcc, v4, v5
	s_addc_u32 s45, s19, 0
	v_ashrrev_i32_e32 v7, 31, v6
	v_cndmask_b32_e32 v4, v2, v4, vcc
	v_lshl_add_u64 v[6:7], v[6:7], 2, s[44:45]
	v_ashrrev_i32_e32 v9, 31, v8
	v_ashrrev_i32_e32 v11, 31, v10
	v_ashrrev_i32_e32 v5, 31, v4
	v_lshl_add_u64 v[8:9], v[8:9], 2, s[44:45]
	v_lshl_add_u64 v[10:11], v[10:11], 2, s[44:45]
	v_lshl_add_u64 v[4:5], v[4:5], 2, s[44:45]
	global_load_dword v12, v[6:7], off
	global_load_dword v13, v[8:9], off
	global_load_dword v14, v[10:11], off
	global_load_dword v15, v[4:5], off
	s_lshl_b32 s18, s18, 21
	v_bfe_u32 v2, v118, 4, 2
	v_ashrrev_i32_e32 v4, 1, v118
	v_bfe_u32 v6, v118, 4, 1
	s_add_u32 s18, s42, s18
	v_bfe_u32 v5, v118, 2, 2
	v_lshlrev_b32_e32 v7, 1, v118
	v_and_b32_e32 v120, 0xffffffc0, v4
	v_lshlrev_b32_e32 v19, 4, v2
	v_lshlrev_b32_e32 v2, 3, v2
	v_lshlrev_b32_e32 v4, 2, v6
	s_addc_u32 s19, s43, 0
	v_lshlrev_b32_e32 v16, 3, v118
	v_ashrrev_i32_e32 v17, 4, v118
	v_and_b32_e32 v7, 0x80, v7
	v_or3_b32 v2, v2, v5, v4
	s_movk_i32 s48, 0x120
	s_add_u32 s44, s18, 0x18dd5100
	v_and_b32_e32 v18, 0x78, v16
	v_lshlrev_b32_e32 v21, 10, v17
	v_mad_u32_u24 v2, v2, s48, v7
	s_addc_u32 s45, s19, 0
	s_lshl_b32 s18, s6, 7
	v_and_b32_e32 v119, 15, v118
	v_and_or_b32 v122, v16, 24, v2
	v_or3_b32 v2, v18, s18, v21
	v_cmp_eq_u32_e32 vcc, 0, v6
	v_or_b32_e32 v6, v120, v119
	v_lshl_add_u64 v[4:5], v[2:3], 1, s[44:45]
	v_cndmask_b32_e32 v20, v236, v237, vcc
	v_lshlrev_b32_e32 v22, 6, v6
	v_add_co_u32_e32 v6, vcc, s40, v4
	s_mov_b32 s18, 0x10000
	s_nop 0
	v_addc_co_u32_e32 v7, vcc, 0, v5, vcc
	v_add_co_u32_e32 v8, vcc, s18, v4
	s_mov_b32 s19, 0x18000
	s_nop 0
	v_addc_co_u32_e32 v9, vcc, 0, v5, vcc
	v_and_b32_e32 v121, 56, v16
	v_add_co_u32_e32 v10, vcc, s19, v4
	v_add_u32_e32 v2, 0x10000, v2
	s_nop 0
	v_addc_co_u32_e32 v11, vcc, 0, v5, vcc
	v_mov_b32_e32 v5, v3
	v_mov_b32_e32 v7, v3
	v_mov_b32_e32 v9, v3
	v_mov_b32_e32 v11, v3
	s_mov_b32 s7, 0
	v_add_u32_e32 v129, v22, v19
	v_add_u32_e32 v130, v122, v20
	s_waitcnt vmcnt(0)
	v_lshlrev_b32_e32 v123, 10, v12
	v_lshlrev_b32_e32 v124, 10, v13
	v_lshlrev_b32_e32 v125, 10, v14
	v_or_b32_e32 v4, v123, v121
	v_lshlrev_b32_e32 v126, 10, v15
	v_or_b32_e32 v6, v124, v121
	v_or_b32_e32 v8, v125, v121
	v_lshl_add_u64 v[4:5], v[4:5], 1, s[28:29]
	v_or_b32_e32 v10, v126, v121
	v_lshl_add_u64 v[6:7], v[6:7], 1, s[28:29]
	v_lshl_add_u64 v[4:5], v[8:9], 1, s[28:29]
	v_lshl_add_u64 v[6:7], v[10:11], 1, s[28:29]
	v_lshl_add_u64 v[4:5], v[2:3], 1, s[44:45]
	v_add_co_u32_e32 v6, vcc, s40, v4
	v_and_b32_e32 v2, 1, v118
	s_nop 0
	v_addc_co_u32_e32 v7, vcc, 0, v5, vcc
	v_add_co_u32_e32 v6, vcc, s18, v4
	v_cmp_eq_u32_e64 s[46:47], 0, v2
	s_nop 0
	v_addc_co_u32_e32 v7, vcc, 0, v5, vcc
	v_add_co_u32_e32 v4, vcc, s19, v4
	v_bfe_i32 v2, v118, 2, 1
	s_nop 0
	v_addc_co_u32_e32 v5, vcc, 0, v5, vcc
	v_and_b32_e32 v2, 0x2040, v2
	v_and_b32_e32 v4, 0xffffffc0, v16
	v_add_u32_e32 v2, v2, v4
	v_lshlrev_b32_e32 v4, 4, v118
	v_and_b32_e32 v5, 48, v4
	v_or3_b32 v4, v21, s15, v18
	v_mul_lo_u32 v6, v17, s48
	v_lshlrev_b32_e32 v7, 4, v119
	v_add_u32_e32 v116, 0x30000, v4
	v_mov_b32_e32 v4, 0
	v_add_u32_e32 v127, v2, v5
	v_add_u32_e32 v128, v6, v7
	s_lshl_b32 s48, s6, 8
	v_lshrrev_b32_e32 v116, 6, v118
	v_lshlrev_b32_e32 v116, 4, v116
	v_bfe_u32 v117, v118, 4, 2
	v_add_u32_e32 v116, v116, v117
	v_mul_u32_u24_e32 v116, 0x800, v116
	v_add_u32_e32 v116, s48, v116
	v_bfe_u32 v68, v118, 1, 3
	v_xor_b32_e32 v68, v68, v117
	v_lshlrev_b32_e32 v68, 1, v68
	v_and_b32_e32 v117, 1, v118
	v_or_b32_e32 v68, v68, v117
	v_lshl_add_u32 v214, v68, 4, v116
	v_add_u32_e32 v215, 0x2000, v214
	v_xor_b32_e32 v68, 8, v68
	v_lshl_add_u32 v216, v68, 4, v116
	v_add_u32_e32 v216, 0x4000, v216
	v_add_u32_e32 v217, 0x2000, v216
	v_lshrrev_b32_e32 v116, 3, v118
	v_lshlrev_b32_e32 v116, 2, v116
	s_barrier
;     ...
;     for (int i = 0; i < 4; ++i) ao[i] = arow((tid >> 3) + 32 * i) + (tid & 7) * 8;
;     const int bk = tid >> 4, bnc = tid & 15;
;     constexpr int NRB = B_F32 ? 8 : 4;
;     u32x4 ra0[4], ra1[4]; u32x4 rb0[NRB], rb1[NRB];
;     auto gloadA = [&](int kt, u32x4 (&ra)[4]) __attribute__((always_inline)) {
; #pragma unroll
;         for (int i = 0; i < 4; ++i) ra[i] = *(const u32x4*)(Abase + (ao[i] + kt * 64));
;     };
;     auto gloadB = [&](int kt, u32x4 (&rb)[NRB]) __attribute__((always_inline)) {
;         if (B_F32) {
;             const float* bp = (const float*)Bbase + (boff + (unsigned)((kt * 64 + bk) * ldb));
; #pragma unroll
;             for (int i = 0; i < 4; ++i) {
;                 if (bval) { rb[2 * i] = *(const u32x4*)(bp + (unsigned)(16 * i * ldb)); rb[2 * i + 1] = *(const u32x4*)(bp + (unsigned)(16 * i * ldb) + 4); }
;                 else { rb[2 * i] = (u32x4){0u, 0u, 0u, 0u}; rb[2 * i + 1] = rb[2 * i]; }
;             }
;         } else {
;             const bf16* bp = (const bf16*)Bbase + (boff + (unsigned)((kt * 64 + bk) * ldb));
; #pragma unroll
;             for (int i = 0; i < 4; ++i) rb[i] = bval ? *(const u32x4*)(bp + (unsigned)(16 * i * ldb)) : (u32x4){0u, 0u, 0u, 0u};
;         }
;     };
;     auto lstore = [&](const u32x4 (&ra)[4], const u32x4 (&rb)[NRB]) __attribute__((always_inline)) {
; #pragma unroll
;         for (int i = 0; i < 4; ++i) { const int row = (tid >> 3) + 32 * i, kc = tid & 7;
;             const u32x4 v = (kc & 1) ? (u32x4){ra[i][2], ra[i][3], ra[i][0], ra[i][1]} : ra[i];
;             *(u32x4*)(lds + (kc >> 2) * GA_KH + row * 64 + (kc & 3) * 16) = v; }
; #pragma unroll
;         for (int i = 0; i < 4; ++i) { const int k = bk + 16 * i;
;             u32x4 v;
;             if (B_F32) { const f32x4 x = __builtin_bit_cast(f32x4, rb[2 * i]), y = __builtin_bit_cast(f32x4, rb[2 * i + 1]);
;                 v[0] = pk2bf(x[0], x[1]); v[1] = pk2bf(x[2], x[3]); v[2] = pk2bf(y[0], y[1]); v[3] = pk2bf(y[2], y[3]); }
;             else v = rb[i];
;             *(u32x4*)(lds + GB_OFF + k * GB_ST + bnc * 16) = v; }
;     };
;     const lds_cptr la = (lds_cptr)lds + (wr * 64 + fr) * 64 + fq * 16;
;     const lds_cptr lb = (lds_cptr)lds + GB_OFF + (8 * fq + (fr >> 2) + (fq & 1) * 4) * GB_ST + wc * 128 + (fr & 3) * 8;
;     const int bsw = (fq & 1) ? -4 * GB_ST : 4 * GB_ST;
	ds_write_b32 v116, v123 offset:36864
	ds_write_b32 v116, v124 offset:36992
	ds_write_b32 v116, v125 offset:37120
	ds_write_b32 v116, v126 offset:37248
	s_waitcnt lgkmcnt(0)
	s_barrier
	v_lshrrev_b32_e32 v117, 6, v118
	v_lshlrev_b32_e32 v117, 5, v117
	v_bfe_u32 v68, v118, 2, 4
	v_add_u32_e32 v117, v117, v68
	v_lshlrev_b32_e32 v117, 2, v117
	ds_read_b32 v123, v117 offset:36864
	ds_read_b32 v125, v117 offset:36928
	v_bfe_u32 v68, v118, 4, 2
	v_sub_u32_e32 v68, 0, v68
	v_and_b32_e32 v68, 3, v68
	v_and_b32_e32 v116, 3, v118
	v_xor_b32_e32 v68, v68, v116
	v_lshlrev_b32_e32 v68, 4, v68
	s_waitcnt lgkmcnt(0)
	v_lshl_add_u32 v123, v123, 1, v68
	v_add_u32_e32 v124, 64, v123
	v_lshl_add_u32 v125, v125, 1, v68
	v_add_u32_e32 v126, 64, v125
	v_bfe_u32 v116, v118, 2, 2
	v_sub_u32_e32 v116, 0, v116
	v_and_b32_e32 v116, 3, v116
	v_lshlrev_b32_e32 v116, 4, v116
	v_xor_b32_e32 v129, v129, v116
	v_bfe_u32 v116, v118, 4, 2
	v_lshlrev_b32_e32 v116, 3, v116
	v_bfe_u32 v117, v118, 2, 2
	v_add_u32_e32 v116, v116, v117
	v_lshlrev_b32_e32 v116, 8, v116
	v_lshrrev_b32_e32 v68, 6, v118
	v_lshrrev_b32_e32 v127, 4, v118
	v_xor_b32_e32 v68, v68, v127
	v_and_b32_e32 v68, 1, v68
	v_lshlrev_b32_e32 v68, 7, v68
	v_or_b32_e32 v116, v116, v68
	v_and_b32_e32 v68, 3, v118
	v_lshlrev_b32_e32 v68, 3, v68
	v_or_b32_e32 v116, v116, v68
	v_xor_b32_e32 v68, 0, v117
	v_lshl_or_b32 v127, v68, 5, v116
	v_xor_b32_e32 v68, 1, v117
	v_lshl_or_b32 v128, v68, 5, v116
	v_xor_b32_e32 v68, 2, v117
	v_lshl_or_b32 v130, v68, 5, v116
	v_xor_b32_e32 v68, 3, v117
	v_lshl_or_b32 v122, v68, 5, v116
	v_lshrrev_b32_e32 v116, 6, v118
	s_nop 1
	v_readfirstlane_b32 s98, v116
	s_nop 1
	s_lshl_b32 s99, s98, 12
	s_lshl_b32 s98, s98, 11
	s_add_u32 m0, s98, 0x0
	s_nop 0
	global_load_lds_dwordx4 v123, s[28:29]
	s_add_u32 m0, s98, 0x2040
	s_nop 0
	global_load_lds_dwordx4 v124, s[28:29]
	s_add_u32 m0, s98, 0x400
	s_nop 0
	global_load_lds_dwordx4 v125, s[28:29]
	s_add_u32 m0, s98, 0x2440
	s_nop 0
	global_load_lds_dwordx4 v126, s[28:29]
	s_add_u32 m0, s99, 0x4080
	s_nop 0
	global_load_lds_dwordx4 v214, s[44:45]
	s_add_u32 m0, s99, 0x4480
	s_nop 0
	global_load_lds_dwordx4 v215, s[44:45]
	s_add_u32 m0, s99, 0x4880
	s_nop 0
	global_load_lds_dwordx4 v216, s[44:45]
	s_add_u32 m0, s99, 0x4c80
	s_nop 0
	global_load_lds_dwordx4 v217, s[44:45]
	s_add_u32 s28, s28, 0x80
	s_addc_u32 s29, s29, 0
	s_add_u32 s44, s44, 0x20000
	s_addc_u32 s45, s45, 0
	s_mov_b32 s7, 0
	v_mov_b32_e32 v5, v4
	v_mov_b32_e32 v6, v4
	v_mov_b32_e32 v7, v4
	v_mov_b32_e32 v16, v4
	v_mov_b32_e32 v17, v4
	v_mov_b32_e32 v18, v4
	v_mov_b32_e32 v19, v4
	v_mov_b32_e32 v8, v4
	v_mov_b32_e32 v9, v4
	v_mov_b32_e32 v10, v4
	v_mov_b32_e32 v11, v4
	v_mov_b32_e32 v12, v4
	v_mov_b32_e32 v13, v4
	v_mov_b32_e32 v14, v4
	v_mov_b32_e32 v15, v4
	v_mov_b32_e32 v20, v4
	v_mov_b32_e32 v21, v4
	v_mov_b32_e32 v22, v4
	v_mov_b32_e32 v23, v4
	v_mov_b32_e32 v60, v4
	v_mov_b32_e32 v61, v4
	v_mov_b32_e32 v62, v4
	v_mov_b32_e32 v63, v4
	v_mov_b32_e32 v28, v4
	v_mov_b32_e32 v29, v4
	v_mov_b32_e32 v30, v4
	v_mov_b32_e32 v31, v4
	v_mov_b32_e32 v72, v4
	v_mov_b32_e32 v73, v4
	v_mov_b32_e32 v74, v4
	v_mov_b32_e32 v75, v4
	v_mov_b32_e32 v84, v4
	v_mov_b32_e32 v85, v4
	v_mov_b32_e32 v86, v4
	v_mov_b32_e32 v87, v4
	v_mov_b32_e32 v92, v4
	v_mov_b32_e32 v93, v4
	v_mov_b32_e32 v94, v4
	v_mov_b32_e32 v95, v4
	v_mov_b32_e32 v88, v4
	v_mov_b32_e32 v89, v4
	v_mov_b32_e32 v90, v4
	v_mov_b32_e32 v91, v4
	v_mov_b32_e32 v96, v4
	v_mov_b32_e32 v97, v4
	v_mov_b32_e32 v98, v4
	v_mov_b32_e32 v99, v4
	v_mov_b32_e32 v100, v4
	v_mov_b32_e32 v101, v4
	v_mov_b32_e32 v102, v4
	v_mov_b32_e32 v103, v4
	v_mov_b32_e32 v108, v4
	v_mov_b32_e32 v109, v4
	v_mov_b32_e32 v110, v4
	v_mov_b32_e32 v111, v4
	v_mov_b32_e32 v104, v4
	v_mov_b32_e32 v105, v4
	v_mov_b32_e32 v106, v4
	v_mov_b32_e32 v107, v4
	v_mov_b32_e32 v112, v4
	v_mov_b32_e32 v113, v4
	v_mov_b32_e32 v114, v4
	v_mov_b32_e32 v115, v4
	s_waitcnt vmcnt(0)
	s_barrier
